# GEMM prologues: all 14 staging pieces of K-tiles 0 and 1 issued before the first counted wait (vmcnt 8 then 6)
# baseline (speedup 1.0000x reference)
; #define PG8_STAGE(bufoff, gbase, voff) do { _Pragma("unroll") for (int _i = 0; _i < 2; ++_i) \
;         __builtin_amdgcn_global_load_lds((const unsigned*)((const char*)(gbase) + (voff)[_i]), (PG8_LAS unsigned*)(lds + (bufoff) + ldsw + _i * 8192), 16, 0, 0); } while (0)
; #define PG8_WAIT_V(n) asm volatile("s_waitcnt vmcnt(" #n ")" ::: "memory")
; #define PG8_BAR __builtin_amdgcn_s_barrier()
; template <class Epi, class Sched, bool ALIGN_EPI>
; __device__ __forceinline__ void gemm_phase(PG8_LAS unsigned char* lds, const Gemm g, const Sched& S, const Epi& E, const int tid) {
;     ...
;     const char* cA = (const char*)g.A + (size_t)cur.pm * tstepA + PG8_ACOL(cur); const char* cB = (const char*)g.Bt + (size_t)cur.pn * tstepB;
;     S.a_ready(cur);
;     PG8_STAGE(PG8_SB(0, 0), cB, voffB); PG8_STAGE(PG8_SB(0, 1), cB + hstepB, voffB); PG8_STAGE(PG8_SA(0, 0), cA, voffA); PG8_STAGE(PG8_SA(0, 1), cA + hstepA, voffA);
;     if (wr == 1) PG8_BAR;
;     PG8_WAIT_V(2); PG8_BAR;
;     PG8_STAGE(PG8_SB(1, 0), cB + kstepB, voffB); PG8_STAGE(PG8_SA(1, 0), cA + kstepA, voffA); PG8_STAGE(PG8_SB(1, 1), cB + hstepB + kstepB, voffB);
;     PG8_WAIT_V(6); PG8_BAR;
.LBB0_240:
	v_readlane_b32 s8, v252, 43
	v_readlane_b32 s9, v252, 44
	s_add_u32 s8, s8, 0x2cb5c000
	s_addc_u32 s9, s9, 0
	s_lshl_b32 s3, s3, 5
	s_and_b32 s50, s3, 0x60
	s_lshl_b32 s49, s6, 6
	s_lshl_b32 s10, s6, 13
	s_lshl_b32 s11, s50, 7
	s_add_u32 s6, s18, 0x8000
	v_mov_b32_e32 v151, v129
	s_addc_u32 s7, s19, 0
	s_add_i32 m0, s45, 0x18000
	v_lshl_add_u64 v[8:9], s[6:7], 0, v[150:151]
	v_mov_b32_e32 v147, v129
	global_load_lds_dwordx4 v[8:9], off
	s_add_i32 m0, s45, 0x1a000
	v_lshl_add_u64 v[8:9], s[6:7], 0, v[146:147]
	s_add_u32 s6, s16, 0x8000
	v_mov_b32_e32 v153, v129
	s_addc_u32 s7, s17, 0
	s_add_i32 s51, s45, 0x8000
	v_mov_b32_e32 v149, v129
	global_load_lds_dwordx4 v[8:9], off
	v_lshl_add_u64 v[8:9], s[6:7], 0, v[152:153]
	s_mov_b32 m0, s51
	s_add_i32 s52, s45, 0xa000
	global_load_lds_dwordx4 v[8:9], off
	v_lshl_add_u64 v[8:9], s[6:7], 0, v[148:149]
	s_add_u32 s6, s18, 0xc000
	s_mov_b32 m0, s52
	s_addc_u32 s7, s19, 0
	global_load_lds_dwordx4 v[8:9], off
	s_add_i32 m0, s45, 0x1c000
	v_lshl_add_u64 v[8:9], s[6:7], 0, v[150:151]
	global_load_lds_dwordx4 v[8:9], off
	v_lshl_add_u64 v[8:9], s[6:7], 0, v[146:147]
	s_add_i32 m0, s45, 0x1e000
	v_and_b32_e32 v7, 15, v1
	global_load_lds_dwordx4 v[8:9], off
	v_lshrrev_b32_e32 v8, 1, v1
	v_and_b32_e32 v9, 24, v8
	v_lshlrev_b32_e32 v8, 1, v9
	v_lshlrev_b32_e32 v1, 2, v1
	s_cmpk_lt_u32 s2, 0x100
	v_lshl_or_b32 v8, v7, 6, v8
	v_and_b32_e32 v1, 32, v1
	s_cselect_b64 s[6:7], -1, 0
	s_and_b32 s2, s49, 0xc0
	v_bitop3_b32 v10, v8, s10, v1 bitop3:0xde
	v_bitop3_b32 v178, s11, v8, v1 bitop3:0xf6
	v_or_b32_e32 v1, s2, v7
	v_lshlrev_b32_e32 v128, 7, v1
	v_lshlrev_b32_e32 v1, 10, v5
	v_and_b32_e32 v1, 0xfffff800, v1
	s_add_i32 s53, s49, 0x80
	v_lshl_add_u32 v1, v4, 7, v1
	v_and_b32_e32 v4, 1, v5
	s_and_b32 s2, s53, 0xc0
	v_lshl_or_b32 v1, v4, 6, v1
	v_or_b32_e32 v171, s49, v7
	v_or_b32_e32 v7, s2, v7
	s_lshl_b32 s2, s50, 2
	v_lshl_add_u32 v158, v6, 1, v1
	v_lshlrev_b32_e32 v1, 10, v0
	s_add_i32 s2, s2, 0
	v_and_b32_e32 v1, 0xfffff800, v1
	s_waitcnt vmcnt(8)
	s_barrier
	s_waitcnt vmcnt(6)
	s_add_i32 s2, s2, 0x23800
	v_lshl_add_u32 v1, v2, 7, v1
	v_and_b32_e32 v0, 1, v0
	v_and_or_b32 v8, s3, 32, v9
	v_lshl_add_u32 v179, v9, 2, s2
	v_lshl_add_u64 v[154:155], s[8:9], 0, v[128:129]
	v_lshlrev_b32_e32 v128, 7, v7
	v_lshl_or_b32 v0, v0, 6, v1
	v_readlane_b32 s2, v251, 12
	v_lshl_add_u64 v[156:157], s[8:9], 0, v[128:129]
	v_mov_b32_e32 v159, v129
	v_lshl_add_u32 v160, v3, 1, v0
	v_mov_b32_e32 v161, v129
	s_mov_b32 s56, 0
	v_add_u32_e32 v180, 0, v10
	v_lshlrev_b32_e32 v128, 1, v8
	v_readlane_b32 s57, v251, 11
	s_mov_b32 s55, s2
	s_barrier
	v_readlane_b32 s3, v251, 13
	s_branch .LBB0_243

; #define PG8_STAGE(bufoff, gbase, voff) do { _Pragma("unroll") for (int _i = 0; _i < 2; ++_i) \
;         __builtin_amdgcn_global_load_lds((const unsigned*)((const char*)(gbase) + (voff)[_i]), (PG8_LAS unsigned*)(lds + (bufoff) + ldsw + _i * 8192), 16, 0, 0); } while (0)
; #define PG8_WAIT_V(n) asm volatile("s_waitcnt vmcnt(" #n ")" ::: "memory")
; #define PG8_BAR __builtin_amdgcn_s_barrier()
; template <class Epi, class Sched, bool ALIGN_EPI>
; __device__ __forceinline__ void gemm_phase(PG8_LAS unsigned char* lds, const Gemm g, const Sched& S, const Epi& E, const int tid) {
;     ...
;     const char* cA = (const char*)g.A + (size_t)cur.pm * tstepA + PG8_ACOL(cur); const char* cB = (const char*)g.Bt + (size_t)cur.pn * tstepB;
;     S.a_ready(cur);
;     PG8_STAGE(PG8_SB(0, 0), cB, voffB); PG8_STAGE(PG8_SB(0, 1), cB + hstepB, voffB); PG8_STAGE(PG8_SA(0, 0), cA, voffA); PG8_STAGE(PG8_SA(0, 1), cA + hstepA, voffA);
;     if (wr == 1) PG8_BAR;
;     PG8_WAIT_V(2); PG8_BAR;
;     PG8_STAGE(PG8_SB(1, 0), cB + kstepB, voffB); PG8_STAGE(PG8_SA(1, 0), cA + kstepA, voffA); PG8_STAGE(PG8_SB(1, 1), cB + hstepB + kstepB, voffB);
;     PG8_WAIT_V(6); PG8_BAR;
.LBB0_336:
	s_and_b64 s[16:17], s[18:19], exec
	s_cselect_b32 s17, 0, s29
	s_cselect_b32 s16, 0, s28
	s_cselect_b32 s45, s61, 0
	s_cselect_b32 s44, s60, 0
	s_lshl_b32 s2, s2, 5
	s_and_b32 s7, s2, 0x60
	s_lshl_b32 s5, s6, 13
	s_lshl_b32 s9, s7, 7
	s_add_u32 s2, s12, 0x8000
	v_mov_b32_e32 v157, v129
	s_addc_u32 s3, s13, 0
	s_add_i32 m0, s62, 0x18000
	v_lshl_add_u64 v[8:9], s[2:3], 0, v[156:157]
	v_mov_b32_e32 v161, v129
	global_load_lds_dwordx4 v[8:9], off
	s_add_i32 m0, s62, 0x1a000
	v_lshl_add_u64 v[8:9], s[2:3], 0, v[160:161]
	s_add_u32 s2, s10, 0x8000
	v_mov_b32_e32 v155, v129
	s_addc_u32 s3, s11, 0
	s_add_i32 s66, s62, 0x8000
	v_mov_b32_e32 v159, v129
	global_load_lds_dwordx4 v[8:9], off
	v_lshl_add_u64 v[8:9], s[2:3], 0, v[154:155]
	s_mov_b32 m0, s66
	s_add_i32 s67, s62, 0xa000
	global_load_lds_dwordx4 v[8:9], off
	v_lshl_add_u64 v[8:9], s[2:3], 0, v[158:159]
	s_add_u32 s2, s12, 0xc000
	s_mov_b32 m0, s67
	s_addc_u32 s3, s13, 0
	global_load_lds_dwordx4 v[8:9], off
	s_add_i32 m0, s62, 0x1c000
	v_lshl_add_u64 v[8:9], s[2:3], 0, v[156:157]
	global_load_lds_dwordx4 v[8:9], off
	v_lshl_add_u64 v[8:9], s[2:3], 0, v[160:161]
	s_add_i32 m0, s62, 0x1e000
	v_and_b32_e32 v7, 15, v0
	global_load_lds_dwordx4 v[8:9], off
	v_bfe_u32 v8, v0, 4, 2
	v_lshlrev_b32_e32 v9, 4, v8
	v_lshlrev_b32_e32 v0, 2, v0
	s_cmpk_lt_u32 s4, 0x100
	v_lshl_or_b32 v9, v7, 6, v9
	v_and_b32_e32 v0, 32, v0
	s_cselect_b64 s[34:35], -1, 0
	s_lshl_b32 s70, s36, 2
	s_lshl_b32 s71, s36, 3
	v_readlane_b32 s36, v252, 43
	v_bitop3_b32 v10, v9, s5, v0 bitop3:0xde
	v_bitop3_b32 v171, s9, v9, v0 bitop3:0xf6
	v_lshl_or_b32 v162, v8, 3, s7
	v_or_b32_e32 v0, v8, v7
	s_ashr_i32 s7, s6, 31
	v_lshlrev_b32_e32 v128, 5, v8
	v_readlane_b32 s37, v252, 44
	v_lshl_or_b32 v163, s6, 6, v7
	v_cmp_eq_u32_e64 s[2:3], 0, v0
	s_lshl_b64 s[6:7], s[6:7], 18
	v_lshl_add_u64 v[8:9], s[36:37], 0, v[128:129]
	s_mov_b64 s[36:37], 0x55c000
	v_cvt_f32_ubyte0_e32 v0, s71
	v_lshl_add_u64 v[164:165], v[8:9], 0, s[36:37]
	s_and_b64 s[36:37], s[18:19], exec
	s_movk_i32 s9, 0x900
	v_rcp_iflag_f32_e32 v0, v0
	s_cselect_b32 s72, 0x1000, s9
	s_cmp_lg_u64 s[44:45], 0
	s_cselect_b64 s[36:37], -1, 0
	s_cmp_lg_u64 s[16:17], 0
	s_cselect_b64 s[38:39], -1, 0
	s_cmp_lg_u32 s68, 2
	s_cselect_b64 s[40:41], -1, 0
	s_add_u32 s73, s60, s6
	v_mul_f32_e32 v0, 0x4f7ffffe, v0
	s_addc_u32 s74, s61, s7
	v_cvt_u32_f32_e32 v0, v0
	s_add_u32 s75, s44, s6
	s_addc_u32 s76, s45, s7
	s_and_b64 s[6:7], s[18:19], exec
	v_readfirstlane_b32 s7, v0
	v_lshlrev_b32_e32 v0, 10, v1
	v_and_b32_e32 v0, 0xfffff800, v0
	v_lshl_add_u32 v0, v2, 7, v0
	v_and_b32_e32 v1, 1, v1
	v_lshl_or_b32 v0, v1, 6, v0
	v_lshl_add_u32 v176, v3, 1, v0
	v_lshlrev_b32_e32 v0, 10, v4
	s_cselect_b32 s77, 11, 8
	s_sub_i32 s6, 0, s71
	v_and_b32_e32 v0, 0xfffff800, v0
	s_waitcnt vmcnt(8)
	s_barrier
	s_waitcnt vmcnt(6)
	s_mul_i32 s6, s6, s7
	v_lshl_add_u32 v0, v5, 7, v0
	v_and_b32_e32 v1, 1, v4
	s_mul_hi_u32 s6, s7, s6
	v_lshl_or_b32 v0, v1, 6, v0
	s_mov_b32 s69, 0
	v_cmp_eq_u32_e64 s[4:5], 0, v7
	s_add_i32 s78, s7, s6
	v_mov_b32_e32 v177, v129
	v_lshl_add_u32 v178, v6, 1, v0
	v_mov_b32_e32 v179, v129
	v_add_u32_e32 v210, 0, v10
	v_lshlrev_b32_e32 v128, 1, v162
	s_barrier
	s_branch .LBB0_339

; #define PG8_STAGE(bufoff, gbase, voff) do { _Pragma("unroll") for (int _i = 0; _i < 2; ++_i) \
;         __builtin_amdgcn_global_load_lds((const unsigned*)((const char*)(gbase) + (voff)[_i]), (PG8_LAS unsigned*)(lds + (bufoff) + ldsw + _i * 8192), 16, 0, 0); } while (0)
; #define PG8_WAIT_V(n) asm volatile("s_waitcnt vmcnt(" #n ")" ::: "memory")
; #define PG8_BAR __builtin_amdgcn_s_barrier()
; template <class Epi, class Sched, bool ALIGN_EPI>
; __device__ __forceinline__ void gemm_phase(PG8_LAS unsigned char* lds, const Gemm g, const Sched& S, const Epi& E, const int tid) {
;     ...
;     const char* cA = (const char*)g.A + (size_t)cur.pm * tstepA + PG8_ACOL(cur); const char* cB = (const char*)g.Bt + (size_t)cur.pn * tstepB;
;     S.a_ready(cur);
;     PG8_STAGE(PG8_SB(0, 0), cB, voffB); PG8_STAGE(PG8_SB(0, 1), cB + hstepB, voffB); PG8_STAGE(PG8_SA(0, 0), cA, voffA); PG8_STAGE(PG8_SA(0, 1), cA + hstepA, voffA);
;     if (wr == 1) PG8_BAR;
;     PG8_WAIT_V(2); PG8_BAR;
;     PG8_STAGE(PG8_SB(1, 0), cB + kstepB, voffB); PG8_STAGE(PG8_SA(1, 0), cA + kstepA, voffA); PG8_STAGE(PG8_SB(1, 1), cB + hstepB + kstepB, voffB);
;     PG8_WAIT_V(6); PG8_BAR;
.LBB0_1380:
	s_lshl_b64 s[8:9], s[60:61], 13
	v_readlane_b32 s16, v252, 43
	v_readlane_b32 s17, v252, 44
	s_add_u32 s7, s16, s8
	s_addc_u32 s8, s17, s9
	s_add_u32 s10, s7, 0x4c0000
	s_addc_u32 s11, s8, 0
	s_add_u32 s12, s16, 0x55c000
	v_readlane_b32 s14, v252, 49
	s_addc_u32 s13, s17, 0
	s_and_b32 s36, s5, 3
	s_lshr_b32 s37, s50, 6
	v_readlane_b32 s15, v252, 50
	s_and_b64 s[8:9], exec, s[14:15]
	s_cselect_b32 s38, s89, 0x8000
	s_lshl_b32 s5, s6, 6
	s_lshl_b32 s8, s6, 13
	s_lshl_b32 s39, s36, 5
	s_lshl_b32 s9, s36, 12
	s_add_u32 s6, s20, 0x8000
	v_mov_b32_e32 v179, v129
	s_addc_u32 s7, s21, 0
	s_add_i32 m0, s31, 0x18000
	v_lshl_add_u64 v[2:3], s[6:7], 0, v[178:179]
	v_mov_b32_e32 v183, v129
	global_load_lds_dwordx4 v[2:3], off
	s_add_i32 m0, s31, 0x1a000
	v_lshl_add_u64 v[2:3], s[6:7], 0, v[182:183]
	s_add_u32 s6, s18, s38
	v_mov_b32_e32 v177, v129
	s_addc_u32 s7, s19, 0
	s_add_i32 s40, s31, 0x8000
	v_mov_b32_e32 v181, v129
	global_load_lds_dwordx4 v[2:3], off
	v_lshl_add_u64 v[2:3], s[6:7], 0, v[176:177]
	s_mov_b32 m0, s40
	s_add_i32 s41, s31, 0xa000
	global_load_lds_dwordx4 v[2:3], off
	v_lshl_add_u64 v[2:3], s[6:7], 0, v[180:181]
	s_add_u32 s6, s20, 0xc000
	s_mov_b32 m0, s41
	s_addc_u32 s7, s21, 0
	global_load_lds_dwordx4 v[2:3], off
	s_add_i32 m0, s31, 0x1c000
	v_lshl_add_u64 v[2:3], s[6:7], 0, v[178:179]
	global_load_lds_dwordx4 v[2:3], off
	v_lshl_add_u64 v[2:3], s[6:7], 0, v[182:183]
	s_add_i32 m0, s31, 0x1e000
	s_lshl_b32 s43, s50, 1
	global_load_lds_dwordx4 v[2:3], off
	s_and_b64 s[6:7], exec, s[14:15]
	v_bfe_u32 v1, v0, 4, 2
	s_cselect_b32 s44, 7, 15
	s_cmpk_lt_u32 s4, 0x100
	v_and_b32_e32 v2, 15, v0
	v_lshlrev_b32_e32 v3, 4, v1
	v_lshlrev_b32_e32 v0, 2, v0
	s_cselect_b64 s[14:15], -1, 0
	s_ashr_i32 s4, s5, 31
	v_or_b32_e32 v184, s5, v2
	v_lshl_or_b32 v2, v2, 6, v3
	v_and_b32_e32 v0, 32, v0
	v_mov_b32_e32 v185, s4
	v_lshlrev_b32_e32 v194, 3, v1
	v_bitop3_b32 v3, v2, s8, v0 bitop3:0xde
	v_bitop3_b32 v195, v2, s9, v0 bitop3:0xde
	s_waitcnt vmcnt(8)
	s_barrier
	s_waitcnt vmcnt(6)
	v_cmp_eq_u32_e64 s[4:5], 0, v1
	v_lshlrev_b64 v[0:1], 7, v[184:185]
	v_lshl_add_u64 v[0:1], s[16:17], 0, v[0:1]
	s_mov_b64 s[6:7], 0x26b5c000
	s_mov_b32 s42, 0
	v_lshl_add_u64 v[186:187], v[0:1], 0, s[6:7]
	s_add_u32 s45, s37, -2
	v_add_u32_e32 v185, 0, v3
	v_readlane_b32 s48, v251, 40
	v_readlane_b32 s49, v251, 35
	s_barrier
	s_branch .LBB0_1383
